# P8 K-loop: two A half-tile LDS-DMAs per 6-DMA load interval issued inside the following MFMA interval; waits recounted 8 to 6
# speedup vs baseline: 1.0070x; 1.0052x over previous
; #define PG8_STAGE(bufoff, gbase, voff) do { PG8_GLDS((const char*)(gbase), (voff)[0], ldsb + (bufoff)); PG8_GLDS((const char*)(gbase), (voff)[1], ldsb + (bufoff) + 8192u); } while (0)
; #define PG8_STAGEA(bufoff, gbase, o0, o1) do { PG8_GLDS((const char*)(gbase), (o0), ldsb + (bufoff)); PG8_GLDS((const char*)(gbase), (o1), ldsb + (bufoff) + 8192u); } while (0)
; #define PG8_STAGEA1(bufoff, gbase) do { if constexpr (Sched::GATHER) { PG8_STAGEA(bufoff, gbase, vA2, vA3); } else { PG8_STAGEA(bufoff, (gbase) + hstep, vA0, vA1); } } while (0)
; #define PG8_LDA(dst, b, h) do { if constexpr (F8) { _Pragma("unroll") for (int m = 0; m < 4; ++m) dst##8[m] = PG8_LD32(lds + PG8_SA(b, h) + aoff + m * 2048); } else { \
;         _Pragma("unroll") for (int m = 0; m < 4; ++m) _Pragma("unroll") for (int k = 0; k < 2; ++k) dst[m][k] = *(const LAS bf16x8*)(lds + PG8_SA(b, h) + aoff + m * 2048 + k * 1024); } } while (0)
; #define PG8_LDB(dst, b, h) do { if constexpr (F8) { _Pragma("unroll") for (int n = 0; n < 2; ++n) dst##8[n] = PG8_LD32(lds + PG8_SB(b, h) + boff + n * 2048); } else { \
;         _Pragma("unroll") for (int n = 0; n < 2; ++n) _Pragma("unroll") for (int k = 0; k < 2; ++k) dst[n][k] = *(const LAS bf16x8*)(lds + PG8_SB(b, h) + boff + n * 2048 + k * 1024); } } while (0)
; template <class Epi, class Sched, bool F8 = false, bool PF = false, bool I8 = false, int PID = -1>
; __device__ __forceinline__ void gemm_phase(LAS unsigned char* lds, LAS unsigned char* xlds, const int RP, const int RPB, const int nt, const Sched& S, const Epi& E, const int stagger_ticks) {
;     ...
;             PG8_LDB(B0, 0, 0); PG8_LDB(B1, 0, 1); PG8_SCHED; PG8_LDA(At, 0, 0); PG8_STAGEA1(PG8_SA(1, 1), a1);
;             if (Sched::GATHER) { if (last) { const u32x4 nv = *nslot; vA0 = nv.x; vA1 = nv.y; vA2 = nv.z; vA3 = nv.w; } }
;             PG8_WAIT_VX(); PG8_WAIT_L(0); PG8_BAR; PG8_MMA(0, 0, At, B0); PG8_MMA(0, 1, At, B1); PG8_BAR; PG8_SCHED;
;             if constexpr (Epi::BIAS_DMA) { if (t == 0 && has_next) E.bias_dma(nxt, xlds + 8192 + ((ui + 1) & 1) * Epi::BIAS_STRIDE, wid, lane); }
;             PG8_LDA(At, 0, 1); PG8_STAGE(PG8_SB(0, 0), b2, voffB); PG8_STAGE(PG8_SB(0, 1), b2 + hstepB, voffB); PG8_STAGEA(PG8_SA(0, 0), a2, vA0, vA1);
;             PG8_WAIT_VX(); PG8_WAIT_L(0); PG8_BAR; PG8_MMA(1, 0, At, B0); PG8_MMA(1, 1, At, B1); PG8_BAR; PG8_SCHED;
.LBB0_958:
	s_add_u32 s28, s2, 0x80
	s_addc_u32 s29, s3, 0
	s_and_b64 s[24:25], s[26:27], exec
	s_cselect_b32 s28, s20, s28
	s_cselect_b32 s29, s21, s29
	s_add_u32 s24, s28, 0x80
	s_addc_u32 s25, s29, 0
	s_waitcnt vmcnt(8)
	s_and_b64 s[26:27], s[26:27], exec
	s_waitcnt lgkmcnt(0)
	s_cselect_b32 s26, s8, s23
	s_cselect_b32 s27, s9, s63
	s_add_u32 s30, s26, 0x80
	s_addc_u32 s31, s27, 0
	s_barrier
	s_setprio 1
	s_waitcnt lgkmcnt(6)
	v_mfma_f32_16x16x128_f8f6f4 v[186:189], v[18:25], v[58:65], v[186:189]
	v_mfma_f32_16x16x128_f8f6f4 v[194:197], v[26:33], v[58:65], v[194:197]
	s_waitcnt lgkmcnt(4)
	v_mfma_f32_16x16x128_f8f6f4 v[190:193], v[18:25], v[50:57], v[190:193]
	v_mfma_f32_16x16x128_f8f6f4 v[182:185], v[26:33], v[50:57], v[182:185]
	s_waitcnt lgkmcnt(2)
	v_mfma_f32_16x16x128_f8f6f4 v[154:157], v[18:25], v[42:49], v[154:157]
	v_mfma_f32_16x16x128_f8f6f4 v[150:153], v[26:33], v[42:49], v[150:153]
	s_waitcnt lgkmcnt(0)
	v_mfma_f32_16x16x128_f8f6f4 v[138:141], v[18:25], v[34:41], v[138:141]
	v_mfma_f32_16x16x128_f8f6f4 v[134:137], v[26:33], v[34:41], v[134:137]
	s_setprio 0
	s_setprio 1
	v_mfma_f32_16x16x128_f8f6f4 v[174:177], v[2:9], v[58:65], v[174:177]
	v_mfma_f32_16x16x128_f8f6f4 v[178:181], v[10:17], v[58:65], v[178:181]
	v_mfma_f32_16x16x128_f8f6f4 v[170:173], v[2:9], v[50:57], v[170:173]
	v_mfma_f32_16x16x128_f8f6f4 v[166:169], v[10:17], v[50:57], v[166:169]
	v_mfma_f32_16x16x128_f8f6f4 v[162:165], v[2:9], v[42:49], v[162:165]
	v_mfma_f32_16x16x128_f8f6f4 v[158:161], v[10:17], v[42:49], v[158:161]
	v_mfma_f32_16x16x128_f8f6f4 v[146:149], v[2:9], v[34:41], v[146:149]
	v_mfma_f32_16x16x128_f8f6f4 v[142:145], v[10:17], v[34:41], v[142:145]
	s_setprio 0
	s_barrier
	ds_read_b128 v[34:37], v207 offset:16384
	ds_read_b128 v[38:41], v207 offset:17408
	ds_read_b128 v[42:45], v207 offset:18432
	ds_read_b128 v[46:49], v207 offset:19456
	ds_read_b128 v[50:53], v207 offset:20480
	ds_read_b128 v[54:57], v207 offset:21504
	ds_read_b128 v[58:61], v207 offset:22528
	ds_read_b128 v[62:65], v207 offset:23552
	s_add_i32 s66, s65, 0x10000
	s_mov_b32 m0, s66
	s_nop 0
	global_load_lds_dwordx4 v204, s[26:27]
	s_add_i32 s66, s65, 0x12000
	s_mov_b32 m0, s66
	s_nop 0
	global_load_lds_dwordx4 v205, s[26:27]
	s_add_u32 s66, s26, 0x2000
	s_addc_u32 s67, s27, 0
	s_add_i32 s68, s65, 0x14000
	s_mov_b32 m0, s68
	s_nop 0
	global_load_lds_dwordx4 v204, s[66:67]
	s_add_i32 s68, s65, 0x16000
	s_mov_b32 m0, s68
	s_nop 0
	global_load_lds_dwordx4 v205, s[66:67]
	s_waitcnt vmcnt(6)
	s_waitcnt lgkmcnt(0)
	s_barrier
	s_setprio 1
	s_waitcnt lgkmcnt(6)
	v_mfma_f32_16x16x128_f8f6f4 v[122:125], v[18:25], v[34:41], v[122:125]
	v_mfma_f32_16x16x128_f8f6f4 v[118:121], v[26:33], v[34:41], v[118:121]
	s_waitcnt lgkmcnt(4)
	v_mfma_f32_16x16x128_f8f6f4 v[106:109], v[18:25], v[42:49], v[106:109]
	v_mfma_f32_16x16x128_f8f6f4 v[102:105], v[26:33], v[42:49], v[102:105]
	s_mov_b32 m0, s65
	s_nop 0
	global_load_lds_dwordx4 v66, s[28:29]
	s_waitcnt lgkmcnt(2)
	v_mfma_f32_16x16x128_f8f6f4 v[90:93], v[18:25], v[50:57], v[90:93]
	v_mfma_f32_16x16x128_f8f6f4 v[86:89], v[26:33], v[50:57], v[86:89]
	s_waitcnt lgkmcnt(0)
	v_mfma_f32_16x16x128_f8f6f4 v[74:77], v[18:25], v[58:65], v[74:77]
	v_mfma_f32_16x16x128_f8f6f4 v[70:73], v[26:33], v[58:65], v[70:73]
	s_setprio 0
	s_setprio 1
	v_mfma_f32_16x16x128_f8f6f4 v[130:133], v[2:9], v[34:41], v[130:133]
	v_mfma_f32_16x16x128_f8f6f4 v[126:129], v[10:17], v[34:41], v[126:129]
	v_mfma_f32_16x16x128_f8f6f4 v[114:117], v[2:9], v[42:49], v[114:117]
	v_mfma_f32_16x16x128_f8f6f4 v[110:113], v[10:17], v[42:49], v[110:113]
	s_add_i32 s98, s65, 0x2000
	s_mov_b32 m0, s98
	s_nop 0
	global_load_lds_dwordx4 v67, s[28:29]
	v_mfma_f32_16x16x128_f8f6f4 v[98:101], v[2:9], v[50:57], v[98:101]
	v_mfma_f32_16x16x128_f8f6f4 v[94:97], v[10:17], v[50:57], v[94:97]
	v_mfma_f32_16x16x128_f8f6f4 v[82:85], v[2:9], v[58:65], v[82:85]
	v_mfma_f32_16x16x128_f8f6f4 v[78:81], v[10:17], v[58:65], v[78:81]
	s_setprio 0
	s_barrier
; #define PG8_STAGE(bufoff, gbase, voff) do { PG8_GLDS((const char*)(gbase), (voff)[0], ldsb + (bufoff)); PG8_GLDS((const char*)(gbase), (voff)[1], ldsb + (bufoff) + 8192u); } while (0)
; #define PG8_STAGEA(bufoff, gbase, o0, o1) do { PG8_GLDS((const char*)(gbase), (o0), ldsb + (bufoff)); PG8_GLDS((const char*)(gbase), (o1), ldsb + (bufoff) + 8192u); } while (0)
; #define PG8_STAGEA1(bufoff, gbase) do { if constexpr (Sched::GATHER) { PG8_STAGEA(bufoff, gbase, vA2, vA3); } else { PG8_STAGEA(bufoff, (gbase) + hstep, vA0, vA1); } } while (0)
; #define PG8_LDA(dst, b, h) do { if constexpr (F8) { _Pragma("unroll") for (int m = 0; m < 4; ++m) dst##8[m] = PG8_LD32(lds + PG8_SA(b, h) + aoff + m * 2048); } else { \
;         _Pragma("unroll") for (int m = 0; m < 4; ++m) _Pragma("unroll") for (int k = 0; k < 2; ++k) dst[m][k] = *(const LAS bf16x8*)(lds + PG8_SA(b, h) + aoff + m * 2048 + k * 1024); } } while (0)
; #define PG8_LDB(dst, b, h) do { if constexpr (F8) { _Pragma("unroll") for (int n = 0; n < 2; ++n) dst##8[n] = PG8_LD32(lds + PG8_SB(b, h) + boff + n * 2048); } else { \
;         _Pragma("unroll") for (int n = 0; n < 2; ++n) _Pragma("unroll") for (int k = 0; k < 2; ++k) dst[n][k] = *(const LAS bf16x8*)(lds + PG8_SB(b, h) + boff + n * 2048 + k * 1024); } } while (0)
; #define PG8_WAIT_VR() PG8_WAIT_V(8)
; #define PG8_WAIT_L(n) asm volatile("s_waitcnt lgkmcnt(" #n ")" ::: "memory")
; #define PG8_BAR __builtin_amdgcn_s_barrier()
; #define PG8_SCHED __builtin_amdgcn_sched_barrier(0)
; template <class Epi, class Sched, bool F8 = false, bool PF = false, bool I8 = false, int PID = -1>
; __device__ __forceinline__ void gemm_phase(LAS unsigned char* lds, LAS unsigned char* xlds, const int RP, const int RPB, const int nt, const Sched& S, const Epi& E, const int stagger_ticks) {
;     ...
;         for (int t = 0; t < nt; t += 2) {
;     ...
;             PG8_LDB(B0, 1, 0); PG8_LDB(B1, 1, 1); PG8_SCHED; PG8_LDA(At, 1, 0); PG8_STAGEA1(PG8_SA(0, 1), a2);
;             PG8_WAIT_VR(); PG8_WAIT_L(0); PG8_BAR; PG8_MMA(0, 0, At, B0); PG8_MMA(0, 1, At, B1); PG8_BAR; PG8_SCHED;
;             PG8_LDA(At, 1, 1); PG8_STAGE(PG8_SB(1, 0), b3, voffB); PG8_STAGE(PG8_SB(1, 1), b3 + hstepB, voffB); PG8_STAGEA(PG8_SA(1, 0), a3, vA0, vA1);
;             PG8_WAIT_VR(); PG8_WAIT_L(0); PG8_BAR; PG8_MMA(1, 0, At, B0); PG8_MMA(1, 1, At, B1); PG8_BAR; PG8_SCHED;
	v_add_u32_e32 v14, 0x18000, v206
	v_add_u32_e32 v30, 0x1c000, v206
	ds_read_b128 v[2:5], v14
	ds_read_b128 v[6:9], v14 offset:1024
	ds_read_b128 v[10:13], v14 offset:2048
	ds_read_b128 v[14:17], v14 offset:3072
	ds_read_b128 v[18:21], v30
	ds_read_b128 v[22:25], v30 offset:1024
	ds_read_b128 v[26:29], v30 offset:2048
	ds_read_b128 v[30:33], v30 offset:3072
	ds_read_b128 v[34:37], v207 offset:32768
	ds_read_b128 v[38:41], v207 offset:33792
	ds_read_b128 v[42:45], v207 offset:34816
	ds_read_b128 v[46:49], v207 offset:35840
	ds_read_b128 v[50:53], v207 offset:36864
	ds_read_b128 v[54:57], v207 offset:37888
	ds_read_b128 v[58:61], v207 offset:38912
	ds_read_b128 v[62:65], v207 offset:39936
	s_add_i32 s66, s65, 0x4000
	s_mov_b32 m0, s66
	s_nop 0
	global_load_lds_dwordx4 v68, s[28:29]
	s_add_i32 s66, s65, 0x6000
	s_mov_b32 m0, s66
	s_nop 0
	global_load_lds_dwordx4 v69, s[28:29]
	s_waitcnt vmcnt(8)
	s_waitcnt lgkmcnt(0)
	s_barrier
	s_setprio 1
	s_waitcnt lgkmcnt(6)
	v_mfma_f32_16x16x128_f8f6f4 v[186:189], v[2:9], v[34:41], v[186:189]
	v_mfma_f32_16x16x128_f8f6f4 v[194:197], v[10:17], v[34:41], v[194:197]
	s_waitcnt lgkmcnt(4)
	v_mfma_f32_16x16x128_f8f6f4 v[190:193], v[2:9], v[42:49], v[190:193]
	v_mfma_f32_16x16x128_f8f6f4 v[182:185], v[10:17], v[42:49], v[182:185]
	s_waitcnt lgkmcnt(2)
	v_mfma_f32_16x16x128_f8f6f4 v[154:157], v[2:9], v[50:57], v[154:157]
	v_mfma_f32_16x16x128_f8f6f4 v[150:153], v[10:17], v[50:57], v[150:153]
	s_waitcnt lgkmcnt(0)
	v_mfma_f32_16x16x128_f8f6f4 v[138:141], v[2:9], v[58:65], v[138:141]
	v_mfma_f32_16x16x128_f8f6f4 v[134:137], v[10:17], v[58:65], v[134:137]
	s_setprio 0
	s_setprio 1
	v_mfma_f32_16x16x128_f8f6f4 v[174:177], v[18:25], v[34:41], v[174:177]
	v_mfma_f32_16x16x128_f8f6f4 v[178:181], v[26:33], v[34:41], v[178:181]
	v_mfma_f32_16x16x128_f8f6f4 v[170:173], v[18:25], v[42:49], v[170:173]
	v_mfma_f32_16x16x128_f8f6f4 v[166:169], v[26:33], v[42:49], v[166:169]
	v_mfma_f32_16x16x128_f8f6f4 v[162:165], v[18:25], v[50:57], v[162:165]
	v_mfma_f32_16x16x128_f8f6f4 v[158:161], v[26:33], v[50:57], v[158:161]
	v_mfma_f32_16x16x128_f8f6f4 v[146:149], v[18:25], v[58:65], v[146:149]
	v_mfma_f32_16x16x128_f8f6f4 v[142:145], v[26:33], v[58:65], v[142:145]
	s_setprio 0
	s_barrier
	ds_read_b128 v[34:37], v207 offset:49152
	ds_read_b128 v[38:41], v207 offset:50176
	ds_read_b128 v[42:45], v207 offset:51200
	ds_read_b128 v[46:49], v207 offset:52224
	ds_read_b128 v[50:53], v207 offset:53248
	ds_read_b128 v[54:57], v207 offset:54272
	ds_read_b128 v[58:61], v207 offset:55296
	ds_read_b128 v[62:65], v207 offset:56320
	s_add_i32 s28, s65, 0x18000
	s_mov_b32 m0, s28
	s_nop 0
	global_load_lds_dwordx4 v204, s[30:31]
	s_add_i32 s28, s65, 0x1a000
	s_mov_b32 m0, s28
	s_nop 0
	global_load_lds_dwordx4 v205, s[30:31]
	s_add_u32 s26, s26, 0x2080
	s_addc_u32 s27, s27, 0
	s_add_i32 s28, s65, 0x1c000
	s_mov_b32 m0, s28
	s_nop 0
	global_load_lds_dwordx4 v204, s[26:27]
	s_add_i32 s28, s65, 0x1e000
	s_mov_b32 m0, s28
	s_nop 0
	global_load_lds_dwordx4 v205, s[26:27]
	s_waitcnt vmcnt(6)
	s_waitcnt lgkmcnt(0)
	s_barrier
	s_setprio 1
	s_waitcnt lgkmcnt(6)
	v_mfma_f32_16x16x128_f8f6f4 v[122:125], v[2:9], v[34:41], v[122:125]
	v_mfma_f32_16x16x128_f8f6f4 v[118:121], v[10:17], v[34:41], v[118:121]
	s_waitcnt lgkmcnt(4)
	v_mfma_f32_16x16x128_f8f6f4 v[106:109], v[2:9], v[42:49], v[106:109]
	v_mfma_f32_16x16x128_f8f6f4 v[102:105], v[10:17], v[42:49], v[102:105]
	s_add_i32 s98, s65, 0x8000
	s_mov_b32 m0, s98
	s_nop 0
	global_load_lds_dwordx4 v66, s[24:25]
	s_waitcnt lgkmcnt(2)
	v_mfma_f32_16x16x128_f8f6f4 v[90:93], v[2:9], v[50:57], v[90:93]
	v_mfma_f32_16x16x128_f8f6f4 v[86:89], v[10:17], v[50:57], v[86:89]
	s_waitcnt lgkmcnt(0)
	v_mfma_f32_16x16x128_f8f6f4 v[74:77], v[2:9], v[58:65], v[74:77]
	v_mfma_f32_16x16x128_f8f6f4 v[70:73], v[10:17], v[58:65], v[70:73]
	s_setprio 0
	s_setprio 1
	v_mfma_f32_16x16x128_f8f6f4 v[130:133], v[18:25], v[34:41], v[130:133]
	v_mfma_f32_16x16x128_f8f6f4 v[126:129], v[26:33], v[34:41], v[126:129]
	v_mfma_f32_16x16x128_f8f6f4 v[114:117], v[18:25], v[42:49], v[114:117]
	v_mfma_f32_16x16x128_f8f6f4 v[110:113], v[26:33], v[42:49], v[110:113]
	s_add_i32 s98, s65, 0xa000
	s_mov_b32 m0, s98
	s_nop 0
	global_load_lds_dwordx4 v67, s[24:25]
	v_mfma_f32_16x16x128_f8f6f4 v[98:101], v[18:25], v[50:57], v[98:101]
	v_mfma_f32_16x16x128_f8f6f4 v[94:97], v[26:33], v[50:57], v[94:97]
	v_mfma_f32_16x16x128_f8f6f4 v[82:85], v[18:25], v[58:65], v[82:85]
	v_mfma_f32_16x16x128_f8f6f4 v[78:81], v[26:33], v[58:65], v[78:81]
	s_setprio 0
	s_barrier
	s_add_i32 s64, s64, 2
	s_add_u32 s23, s23, 0x100
	s_addc_u32 s63, s63, 0
	s_add_u32 s2, s2, 0x100
	s_addc_u32 s3, s3, 0
	s_cmp_gt_u32 s64, 5
	s_cbranch_scc1 .LBB0_961
